# phase 8 LayerNorm-1: gamma/beta preloaded once before the row loop (were re-loaded per row behind exposed waits), waits recomputed by scoreboard; on top of v43
# speedup vs baseline: 1.0046x; 1.0046x over previous
.LBB0_880:
	s_lshl_b32 s30, s27, 6
	s_add_i32 s72, s30, s71
	s_mov_b32 s6, 0
	s_mov_b64 s[4:5], -1
	global_load_dwordx4 v[182:185], v[72:73], off
	global_load_dwordx4 v[186:189], v[72:73], off offset:16
	global_load_dwordx4 v[190:193], v[74:75], off
	global_load_dwordx4 v[194:197], v[74:75], off offset:16
	global_load_dwordx4 v[198:201], v[72:73], off offset:2048
	global_load_dwordx4 v[202:205], v[72:73], off offset:2064
	global_load_dwordx4 v[206:209], v[74:75], off offset:2048
	global_load_dwordx4 v[212:215], v[74:75], off offset:2064
	global_load_dwordx4 v[216:219], v[76:77], off
	global_load_dwordx4 v[220:223], v[76:77], off offset:16
	global_load_dwordx4 v[224:227], v[78:79], off
	global_load_dwordx4 v[240:243], v[78:79], off offset:16
	global_load_dwordx4 v[244:247], v[80:81], off
	global_load_dwordx4 v[232:235], v[80:81], off offset:16
	global_load_dwordx4 v[236:239], v[82:83], off
	global_load_dwordx4 v[248:251], v[82:83], off offset:16
.LBB0_881:
	s_or_b32 s64, s6, s72
	s_ashr_i32 s65, s64, 31
	s_lshl_b64 s[6:7], s[64:65], 12
	v_lshl_add_u64 v[56:57], v[84:85], 0, s[6:7]
	global_load_dwordx4 v[58:61], v[56:57], off
	global_load_dwordx4 v[62:65], v[56:57], off offset:1024
	global_load_dwordx4 v[166:169], v[56:57], off offset:2048
	global_load_dwordx4 v[170:173], v[56:57], off offset:3072
	s_or_b32 s62, s64, 1
	s_ashr_i32 s63, s62, 31
	s_or_b32 s60, s64, 2
	s_lshl_b64 s[6:7], s[62:63], 12
	s_ashr_i32 s61, s60, 31
	v_lshl_add_u64 v[54:55], v[84:85], 0, s[6:7]
	s_lshl_b64 s[6:7], s[60:61], 12
	v_lshl_add_u64 v[52:53], v[84:85], 0, s[6:7]
	s_or_b32 s6, s64, 3
	s_ashr_i32 s7, s6, 31
	s_lshl_b64 s[20:21], s[6:7], 12
	v_lshl_add_u64 v[50:51], v[84:85], 0, s[20:21]
	global_load_dwordx4 v[46:49], v[54:55], off
	global_load_dwordx4 v[42:45], v[54:55], off offset:1024
	global_load_dwordx4 v[38:41], v[54:55], off offset:2048
	global_load_dwordx4 v[34:37], v[54:55], off offset:3072
	global_load_dwordx4 v[30:33], v[52:53], off
	global_load_dwordx4 v[26:29], v[52:53], off offset:1024
	global_load_dwordx4 v[22:25], v[52:53], off offset:2048
	global_load_dwordx4 v[18:21], v[52:53], off offset:3072
	global_load_dwordx4 v[14:17], v[50:51], off
	global_load_dwordx4 v[10:13], v[50:51], off offset:1024
	global_load_dwordx4 v[6:9], v[50:51], off offset:2048
	global_load_dwordx4 v[2:5], v[50:51], off offset:3072
	s_lshl_b64 s[6:7], s[6:7], 11
	s_waitcnt vmcnt(15)
	v_lshlrev_b32_e32 v164, 16, v58
	v_and_b32_e32 v163, 0xffff0000, v58
	v_lshlrev_b32_e32 v162, 16, v59
	v_and_b32_e32 v161, 0xffff0000, v59
	v_lshlrev_b32_e32 v160, 16, v60
	v_and_b32_e32 v159, 0xffff0000, v60
	v_lshlrev_b32_e32 v111, 16, v61
	v_and_b32_e32 v110, 0xffff0000, v61
	v_add_f32_e32 v0, v164, v163
	v_add_f32_e32 v58, v162, v161
	v_add_f32_e32 v0, v0, v58
	v_add_f32_e32 v58, v160, v159
	v_add_f32_e32 v59, v111, v110
	v_add_f32_e32 v58, v58, v59
	s_waitcnt vmcnt(14)
	v_lshlrev_b32_e32 v109, 16, v62
	v_and_b32_e32 v108, 0xffff0000, v62
	v_lshlrev_b32_e32 v107, 16, v63
	v_and_b32_e32 v106, 0xffff0000, v63
	v_add_f32_e32 v0, v0, v58
	v_lshlrev_b32_e32 v105, 16, v64
	v_and_b32_e32 v104, 0xffff0000, v64
	v_lshlrev_b32_e32 v103, 16, v65
	v_and_b32_e32 v102, 0xffff0000, v65
	v_add_f32_e32 v58, v109, v108
	v_add_f32_e32 v59, v107, v106
	v_add_f32_e32 v58, v58, v59
	v_add_f32_e32 v59, v105, v104
	v_add_f32_e32 v60, v103, v102
	v_add_f32_e32 v59, v59, v60
	v_add_f32_e32 v0, 0, v0
	v_add_f32_e32 v58, v58, v59
	s_waitcnt vmcnt(13)
	v_lshlrev_b32_e32 v101, 16, v166
	v_and_b32_e32 v100, 0xffff0000, v166
	v_lshlrev_b32_e32 v99, 16, v167
	v_and_b32_e32 v98, 0xffff0000, v167
	v_add_f32_e32 v0, v0, v58
	v_lshlrev_b32_e32 v97, 16, v168
	v_and_b32_e32 v96, 0xffff0000, v168
	v_lshlrev_b32_e32 v95, 16, v169
	v_and_b32_e32 v94, 0xffff0000, v169
	v_add_f32_e32 v58, v101, v100
	v_add_f32_e32 v59, v99, v98
	v_add_f32_e32 v58, v58, v59
	v_add_f32_e32 v59, v97, v96
	v_add_f32_e32 v60, v95, v94
	v_add_f32_e32 v59, v59, v60
	v_add_f32_e32 v58, v58, v59
	s_waitcnt vmcnt(12)
	v_lshlrev_b32_e32 v67, 16, v170
	v_and_b32_e32 v65, 0xffff0000, v170
	v_lshlrev_b32_e32 v64, 16, v171
	v_and_b32_e32 v63, 0xffff0000, v171
	v_add_f32_e32 v58, v0, v58
	v_lshlrev_b32_e32 v62, 16, v172
	v_and_b32_e32 v61, 0xffff0000, v172
	v_lshlrev_b32_e32 v60, 16, v173
	v_and_b32_e32 v0, 0xffff0000, v173
	v_add_f32_e32 v59, v67, v65
	v_add_f32_e32 v91, v64, v63
	v_add_f32_e32 v59, v59, v91
	v_add_f32_e32 v91, v62, v61
	v_add_f32_e32 v165, v60, v0
	v_add_f32_e32 v91, v91, v165
	v_add_f32_e32 v59, v59, v91
	v_add_f32_e32 v58, v58, v59
	ds_swizzle_b32 v59, v58 offset:swizzle(SWAP,1)
	s_waitcnt lgkmcnt(0)
	v_add_f32_e32 v58, v58, v59
	ds_swizzle_b32 v59, v58 offset:swizzle(SWAP,2)
	s_waitcnt lgkmcnt(0)
	v_add_f32_e32 v58, v58, v59
	ds_swizzle_b32 v59, v58 offset:swizzle(SWAP,4)
	s_waitcnt lgkmcnt(0)
	v_add_f32_e32 v58, v58, v59
	ds_swizzle_b32 v59, v58 offset:swizzle(SWAP,8)
	s_waitcnt lgkmcnt(0)
	v_add_f32_e32 v58, v58, v59
	ds_swizzle_b32 v59, v58 offset:swizzle(SWAP,16)
	s_waitcnt lgkmcnt(0)
	v_add_f32_e32 v58, v58, v59
	v_mov_b32_e32 v59, v58
	s_nop 1
	v_permlane32_swap_b32_e32 v58, v59
	v_add_f32_e32 v58, v58, v59
	v_fmac_f32_e32 v163, 0xba000000, v58
	v_fmac_f32_e32 v164, 0xba000000, v58
	v_mul_f32_e32 v59, v163, v163
	v_fmac_f32_e32 v59, v164, v164
	v_fmac_f32_e32 v162, 0xba000000, v58
	v_fmac_f32_e32 v59, v162, v162
	v_fmac_f32_e32 v161, 0xba000000, v58
	v_fmac_f32_e32 v59, v161, v161
	v_fmac_f32_e32 v160, 0xba000000, v58
	v_fmac_f32_e32 v59, v160, v160
	v_fmac_f32_e32 v159, 0xba000000, v58
	v_fmac_f32_e32 v59, v159, v159
	v_fmac_f32_e32 v111, 0xba000000, v58
	v_fmac_f32_e32 v59, v111, v111
	v_fmac_f32_e32 v110, 0xba000000, v58
	v_fmac_f32_e32 v59, v110, v110
	v_fmac_f32_e32 v109, 0xba000000, v58
	v_fmac_f32_e32 v59, v109, v109
	v_fmac_f32_e32 v108, 0xba000000, v58
	v_fmac_f32_e32 v59, v108, v108
	v_fmac_f32_e32 v107, 0xba000000, v58
	v_fmac_f32_e32 v59, v107, v107
	v_fmac_f32_e32 v106, 0xba000000, v58
	v_fmac_f32_e32 v59, v106, v106
	v_fmac_f32_e32 v105, 0xba000000, v58
	v_fmac_f32_e32 v59, v105, v105
	v_fmac_f32_e32 v104, 0xba000000, v58
	v_fmac_f32_e32 v59, v104, v104
	v_fmac_f32_e32 v103, 0xba000000, v58
	v_fmac_f32_e32 v59, v103, v103
	v_fmac_f32_e32 v102, 0xba000000, v58
	v_fmac_f32_e32 v59, v102, v102
	v_fmac_f32_e32 v101, 0xba000000, v58
	v_fmac_f32_e32 v59, v101, v101
	v_fmac_f32_e32 v100, 0xba000000, v58
	v_fmac_f32_e32 v59, v100, v100
	v_fmac_f32_e32 v99, 0xba000000, v58
	v_fmac_f32_e32 v59, v99, v99
	v_fmac_f32_e32 v98, 0xba000000, v58
	v_fmac_f32_e32 v59, v98, v98
	v_fmac_f32_e32 v97, 0xba000000, v58
	v_fmac_f32_e32 v59, v97, v97
	v_fmac_f32_e32 v96, 0xba000000, v58
	v_fmac_f32_e32 v59, v96, v96
	v_fmac_f32_e32 v95, 0xba000000, v58
	v_fmac_f32_e32 v59, v95, v95
	v_fmac_f32_e32 v94, 0xba000000, v58
	v_fmac_f32_e32 v59, v94, v94
	v_fmac_f32_e32 v67, 0xba000000, v58
	v_fmac_f32_e32 v59, v67, v67
	v_fmac_f32_e32 v65, 0xba000000, v58
	v_fmac_f32_e32 v59, v65, v65
	v_fmac_f32_e32 v64, 0xba000000, v58
	v_fmac_f32_e32 v59, v64, v64
	v_fmac_f32_e32 v63, 0xba000000, v58
	v_fmac_f32_e32 v59, v63, v63
	v_fmac_f32_e32 v62, 0xba000000, v58
	v_fmac_f32_e32 v59, v62, v62
	v_fmac_f32_e32 v61, 0xba000000, v58
	v_fmac_f32_e32 v59, v61, v61
	v_fmac_f32_e32 v60, 0xba000000, v58
	v_fmac_f32_e32 v59, v60, v60
	v_fmac_f32_e32 v0, 0xba000000, v58
	v_fmac_f32_e32 v59, v0, v0
	ds_swizzle_b32 v58, v59 offset:swizzle(SWAP,1)
	s_waitcnt lgkmcnt(0)
	v_add_f32_e32 v58, v59, v58
	ds_swizzle_b32 v59, v58 offset:swizzle(SWAP,2)
	s_waitcnt lgkmcnt(0)
	v_add_f32_e32 v58, v58, v59
	ds_swizzle_b32 v59, v58 offset:swizzle(SWAP,4)
	s_waitcnt lgkmcnt(0)
	v_add_f32_e32 v58, v58, v59
	ds_swizzle_b32 v59, v58 offset:swizzle(SWAP,8)
	s_waitcnt lgkmcnt(0)
	v_add_f32_e32 v58, v58, v59
	ds_swizzle_b32 v59, v58 offset:swizzle(SWAP,16)
	s_waitcnt lgkmcnt(0)
	v_add_f32_e32 v58, v58, v59
	v_mov_b32_e32 v59, v58
	s_nop 1
	v_permlane32_swap_b32_e32 v58, v59
	v_add_f32_e32 v58, v58, v59
	v_fmamk_f32 v58, v58, 0x3a000000, v210
	v_cmp_gt_f32_e32 vcc, s25, v58
	v_mul_f32_e32 v59, 0x4f800000, v58
	s_nop 0
	v_cndmask_b32_e32 v58, v58, v59, vcc
	v_sqrt_f32_e32 v59, v58
	s_nop 0
	v_add_u32_e32 v91, -1, v59
	v_fma_f32 v165, -v91, v59, v58
	v_cmp_ge_f32_e64 s[58:59], 0, v165
	v_add_u32_e32 v165, 1, v59
	s_nop 0
	v_cndmask_b32_e64 v91, v59, v91, s[58:59]
	v_fma_f32 v59, -v165, v59, v58
	v_cmp_lt_f32_e64 s[58:59], 0, v59
	s_nop 1
	v_cndmask_b32_e64 v59, v91, v165, s[58:59]
	v_mul_f32_e32 v91, 0x37800000, v59
	v_cndmask_b32_e32 v59, v59, v91, vcc
	v_cmp_class_f32_e32 vcc, v58, v211
	s_nop 1
	v_cndmask_b32_e32 v58, v59, v58, vcc
	v_div_scale_f32 v59, s[20:21], v58, v58, 1.0
	v_rcp_f32_e32 v91, v59
	s_lshl_b64 s[20:21], s[64:65], 11
	v_fma_f32 v165, -v59, v91, 1.0
	v_fmac_f32_e32 v91, v165, v91
	v_div_scale_f32 v165, vcc, 1.0, v58, 1.0
	v_mul_f32_e32 v166, v165, v91
	v_fma_f32 v167, -v59, v166, v165
	v_fmac_f32_e32 v166, v167, v91
	v_fma_f32 v59, -v59, v166, v165
	v_div_fmas_f32 v59, v59, v91, v166
	v_div_fixup_f32 v91, v59, v58, 1.0
	v_mul_f32_e32 v164, v164, v91
	v_mul_f32_e32 v163, v163, v91
	v_mul_f32_e32 v160, v160, v91
	v_mul_f32_e32 v162, v162, v91
	v_mul_f32_e32 v161, v161, v91
	v_mul_f32_e32 v159, v159, v91
	v_mul_f32_e32 v111, v111, v91
	v_mul_f32_e32 v110, v110, v91
	v_lshl_add_u64 v[58:59], v[86:87], 0, s[20:21]
	v_mul_f32_e32 v109, v109, v91
	v_mul_f32_e32 v108, v108, v91
	v_mul_f32_e32 v107, v107, v91
	v_mul_f32_e32 v106, v106, v91
	v_mul_f32_e32 v105, v105, v91
	v_mul_f32_e32 v104, v104, v91
	v_mul_f32_e32 v103, v103, v91
	v_mul_f32_e32 v102, v102, v91
	v_mul_f32_e32 v101, v101, v91
	v_mul_f32_e32 v100, v100, v91
	v_mul_f32_e32 v99, v99, v91
	v_mul_f32_e32 v98, v98, v91
	v_mul_f32_e32 v97, v97, v91
	v_mul_f32_e32 v96, v96, v91
	v_mul_f32_e32 v95, v95, v91
	v_mul_f32_e32 v94, v94, v91
	v_mul_f32_e32 v67, v67, v91
	v_mul_f32_e32 v65, v65, v91
	v_mul_f32_e32 v64, v64, v91
	v_mul_f32_e32 v63, v63, v91
	v_mul_f32_e32 v62, v62, v91
	v_mul_f32_e32 v61, v61, v91
	v_mul_f32_e32 v60, v60, v91
	v_mul_f32_e32 v0, v0, v91
	s_waitcnt vmcnt(10)
	v_lshlrev_b32_e32 v91, 16, v45
	s_waitcnt vmcnt(28)
	v_fma_f32 v166, v186, v160, v194
	s_waitcnt vmcnt(11)
	v_fma_f32 v164, v182, v164, v190
	v_fma_f32 v165, v183, v163, v191
	v_cvt_pk_bf16_f32 v160, v164, v165
	v_fma_f32 v170, v184, v162, v192
	v_fma_f32 v181, v185, v161, v193
	v_fma_f32 v159, v187, v159, v195
	v_fma_f32 v167, v188, v111, v196
	v_fma_f32 v177, v189, v110, v197
	v_cvt_pk_bf16_f32 v161, v170, v181
	v_cvt_pk_bf16_f32 v162, v166, v159
	v_cvt_pk_bf16_f32 v163, v167, v177
	global_store_dwordx4 v[56:57], v[160:163], off
	v_med3_f32 v111, v164, s19, v229
	v_mov_b32_e32 v110, v1
	v_med3_f32 v160, v165, s19, v229
	v_cvt_pk_fp8_f32 v110, v111, v160
	v_med3_f32 v111, v170, s19, v229
	v_med3_f32 v160, v181, s19, v229
	v_med3_f32 v159, v159, s19, v229
	v_cvt_pk_fp8_f32 v110, v111, v160 op_sel:[0,0,1]
	v_med3_f32 v160, v166, s19, v229
	v_mov_b32_e32 v111, v1
	v_cvt_pk_fp8_f32 v111, v160, v159
	v_med3_f32 v159, v167, s19, v229
	v_med3_f32 v160, v177, s19, v229
	v_cvt_pk_fp8_f32 v111, v159, v160 op_sel:[0,0,1]
	v_lshlrev_b32_e32 v159, 16, v48
	global_store_dwordx2 v[58:59], v[110:111], off
	s_waitcnt vmcnt(26)
	v_fma_f32 v110, v104, v203, v213
	s_waitcnt vmcnt(27)
	v_fma_f32 v109, v109, v198, v206
	v_fma_f32 v108, v108, v199, v207
	v_fma_f32 v107, v107, v200, v208
	v_fma_f32 v175, v106, v201, v209
	v_fma_f32 v106, v105, v202, v212
	v_fma_f32 v111, v103, v204, v214
	v_fma_f32 v171, v102, v205, v215
	v_cvt_pk_bf16_f32 v102, v109, v108
	v_cvt_pk_bf16_f32 v103, v107, v175
	v_cvt_pk_bf16_f32 v104, v106, v110
	v_cvt_pk_bf16_f32 v105, v111, v171
	global_store_dwordx4 v[56:57], v[102:105], off offset:1024
	s_nop 1
	v_med3_f32 v103, v109, s19, v229
	v_med3_f32 v104, v108, s19, v229
	v_mov_b32_e32 v102, v1
	v_cvt_pk_fp8_f32 v102, v103, v104
	v_med3_f32 v103, v107, s19, v229
	v_med3_f32 v104, v175, s19, v229
	v_med3_f32 v105, v110, s19, v229
	v_cvt_pk_fp8_f32 v102, v103, v104 op_sel:[0,0,1]
	v_med3_f32 v104, v106, s19, v229
	v_mov_b32_e32 v103, v1
	v_cvt_pk_fp8_f32 v103, v104, v105
	v_med3_f32 v104, v111, s19, v229
	v_med3_f32 v105, v171, s19, v229
	v_lshlrev_b32_e32 v110, 16, v47
	v_cvt_pk_fp8_f32 v103, v104, v105 op_sel:[0,0,1]
	v_and_b32_e32 v111, 0xffff0000, v47
	global_store_dwordx2 v[58:59], v[102:103], off offset:512
	s_nop 0
	s_waitcnt vmcnt(24)
	v_fma_f32 v163, v94, v223, v243
	s_waitcnt vmcnt(12)
	v_fma_f32 v101, v101, v216, v224
	v_fma_f32 v100, v100, v217, v225
	v_fma_f32 v99, v99, v218, v226
	v_fma_f32 v167, v98, v219, v227
	v_fma_f32 v98, v97, v220, v240
	v_fma_f32 v102, v96, v221, v241
	v_fma_f32 v103, v95, v222, v242
	v_cvt_pk_bf16_f32 v94, v101, v100
	v_cvt_pk_bf16_f32 v95, v99, v167
	v_cvt_pk_bf16_f32 v96, v98, v102
	v_cvt_pk_bf16_f32 v97, v103, v163
	global_store_dwordx4 v[56:57], v[94:97], off offset:2048
	v_and_b32_e32 v160, 0xffff0000, v48
	v_lshlrev_b32_e32 v161, 16, v49
	v_med3_f32 v95, v101, s19, v229
	v_med3_f32 v96, v100, s19, v229
	v_mov_b32_e32 v94, v1
	v_cvt_pk_fp8_f32 v94, v95, v96
	v_med3_f32 v95, v99, s19, v229
	v_med3_f32 v96, v167, s19, v229
	v_med3_f32 v97, v102, s19, v229
	v_cvt_pk_fp8_f32 v94, v95, v96 op_sel:[0,0,1]
	v_med3_f32 v96, v98, s19, v229
	v_mov_b32_e32 v95, v1
	v_cvt_pk_fp8_f32 v95, v96, v97
	v_med3_f32 v96, v103, s19, v229
	v_med3_f32 v97, v163, s19, v229
	v_and_b32_e32 v162, 0xffff0000, v49
	v_cvt_pk_fp8_f32 v95, v96, v97 op_sel:[0,0,1]
	v_add_f32_e32 v47, v161, v162
	v_and_b32_e32 v49, 0xffff0000, v34
	v_lshlrev_b32_e32 v48, 16, v35
	global_store_dwordx2 v[58:59], v[94:95], off offset:1024
	s_nop 0
	s_waitcnt vmcnt(22)
	v_fma_f32 v94, v62, v232, v248
	s_waitcnt vmcnt(15)
	v_fma_f32 v67, v67, v244, v236
	v_fma_f32 v65, v65, v245, v237
	v_fma_f32 v64, v64, v246, v238
	v_fma_f32 v109, v63, v247, v239
	v_fma_f32 v95, v61, v233, v249
	v_fma_f32 v96, v60, v234, v250
	v_fma_f32 v105, v0, v235, v251
	v_cvt_pk_bf16_f32 v60, v67, v65
	v_cvt_pk_bf16_f32 v61, v64, v109
	v_cvt_pk_bf16_f32 v62, v94, v95
	v_cvt_pk_bf16_f32 v63, v96, v105
	global_store_dwordx4 v[56:57], v[60:63], off offset:3072
	v_med3_f32 v0, v67, s19, v229
	v_med3_f32 v57, v65, s19, v229
	v_mov_b32_e32 v56, v1
	v_cvt_pk_fp8_f32 v56, v0, v57
	v_med3_f32 v0, v64, s19, v229
	v_med3_f32 v57, v109, s19, v229
	v_med3_f32 v60, v95, s19, v229
	v_cvt_pk_fp8_f32 v56, v0, v57 op_sel:[0,0,1]
	v_med3_f32 v0, v94, s19, v229
	v_mov_b32_e32 v57, v1
	v_cvt_pk_fp8_f32 v57, v0, v60
	v_med3_f32 v0, v96, s19, v229
	v_med3_f32 v60, v105, s19, v229
	v_lshlrev_b32_e32 v108, 16, v46
	v_cvt_pk_fp8_f32 v57, v0, v60 op_sel:[0,0,1]
	v_and_b32_e32 v109, 0xffff0000, v46
	v_add_f32_e32 v0, v108, v109
	v_add_f32_e32 v46, v110, v111
	v_lshlrev_b32_e32 v99, 16, v42
	v_and_b32_e32 v98, 0xffff0000, v42
	v_lshlrev_b32_e32 v97, 16, v43
	v_and_b32_e32 v96, 0xffff0000, v43
	v_add_f32_e32 v0, v0, v46
	v_add_f32_e32 v46, v159, v160
	v_lshlrev_b32_e32 v95, 16, v44
	v_and_b32_e32 v94, 0xffff0000, v44
	v_and_b32_e32 v67, 0xffff0000, v45
	v_add_f32_e32 v42, v99, v98
	v_add_f32_e32 v43, v97, v96
	v_lshlrev_b32_e32 v65, 16, v38
	v_and_b32_e32 v64, 0xffff0000, v38
	v_lshlrev_b32_e32 v63, 16, v39
	v_and_b32_e32 v62, 0xffff0000, v39
	global_store_dwordx2 v[58:59], v[56:57], off offset:1536
	v_add_f32_e32 v46, v46, v47
	v_add_f32_e32 v42, v42, v43
	v_add_f32_e32 v43, v95, v94
	v_add_f32_e32 v44, v91, v67
	v_lshlrev_b32_e32 v61, 16, v40
	v_and_b32_e32 v60, 0xffff0000, v40
	v_lshlrev_b32_e32 v59, 16, v41
	v_and_b32_e32 v58, 0xffff0000, v41
	v_add_f32_e32 v38, v65, v64
	v_add_f32_e32 v39, v63, v62
	v_add_f32_e32 v0, v0, v46
	v_add_f32_e32 v43, v43, v44
	v_add_f32_e32 v38, v38, v39
	v_add_f32_e32 v39, v61, v60
	v_add_f32_e32 v40, v59, v58
	v_add_f32_e32 v0, 0, v0
	v_add_f32_e32 v42, v42, v43
	v_add_f32_e32 v39, v39, v40
	v_add_f32_e32 v0, v0, v42
	v_add_f32_e32 v38, v38, v39
	v_lshlrev_b32_e32 v56, 16, v34
	v_and_b32_e32 v47, 0xffff0000, v35
	v_add_f32_e32 v38, v0, v38
	v_lshlrev_b32_e32 v46, 16, v36
	v_and_b32_e32 v45, 0xffff0000, v36
	v_lshlrev_b32_e32 v44, 16, v37
	v_and_b32_e32 v0, 0xffff0000, v37
	v_add_f32_e32 v34, v56, v49
	v_add_f32_e32 v35, v48, v47
	v_add_f32_e32 v34, v34, v35
	v_add_f32_e32 v35, v46, v45
	v_add_f32_e32 v36, v44, v0
	v_add_f32_e32 v35, v35, v36
	v_add_f32_e32 v34, v34, v35
	v_add_f32_e32 v34, v38, v34
	ds_swizzle_b32 v35, v34 offset:swizzle(SWAP,1)
	s_waitcnt lgkmcnt(0)
	v_add_f32_e32 v34, v34, v35
	ds_swizzle_b32 v35, v34 offset:swizzle(SWAP,2)
	s_waitcnt lgkmcnt(0)
	v_add_f32_e32 v34, v34, v35
	ds_swizzle_b32 v35, v34 offset:swizzle(SWAP,4)
	s_waitcnt lgkmcnt(0)
	v_add_f32_e32 v34, v34, v35
	ds_swizzle_b32 v35, v34 offset:swizzle(SWAP,8)
	s_waitcnt lgkmcnt(0)
	v_add_f32_e32 v34, v34, v35
	ds_swizzle_b32 v35, v34 offset:swizzle(SWAP,16)
	s_waitcnt lgkmcnt(0)
	v_add_f32_e32 v34, v34, v35
	v_mov_b32_e32 v35, v34
	s_nop 1
	v_permlane32_swap_b32_e32 v34, v35
	v_add_f32_e32 v34, v34, v35
	v_fmac_f32_e32 v109, 0xba000000, v34
	v_fmac_f32_e32 v108, 0xba000000, v34
	v_mul_f32_e32 v35, v109, v109
	v_fmac_f32_e32 v35, v108, v108
	v_fmac_f32_e32 v110, 0xba000000, v34
	v_fmac_f32_e32 v35, v110, v110
	v_fmac_f32_e32 v111, 0xba000000, v34
	v_fmac_f32_e32 v35, v111, v111
	v_fmac_f32_e32 v159, 0xba000000, v34
	v_fmac_f32_e32 v35, v159, v159
	v_fmac_f32_e32 v160, 0xba000000, v34
	v_fmac_f32_e32 v35, v160, v160
	v_fmac_f32_e32 v161, 0xba000000, v34
	v_fmac_f32_e32 v35, v161, v161
	v_fmac_f32_e32 v162, 0xba000000, v34
	v_fmac_f32_e32 v35, v162, v162
	v_fmac_f32_e32 v99, 0xba000000, v34
	v_fmac_f32_e32 v35, v99, v99
	v_fmac_f32_e32 v98, 0xba000000, v34
	v_fmac_f32_e32 v35, v98, v98
	v_fmac_f32_e32 v97, 0xba000000, v34
	v_fmac_f32_e32 v35, v97, v97
	v_fmac_f32_e32 v96, 0xba000000, v34
	v_fmac_f32_e32 v35, v96, v96
	v_fmac_f32_e32 v95, 0xba000000, v34
	v_fmac_f32_e32 v35, v95, v95
	v_fmac_f32_e32 v94, 0xba000000, v34
	v_fmac_f32_e32 v35, v94, v94
	v_fmac_f32_e32 v91, 0xba000000, v34
	v_fmac_f32_e32 v35, v91, v91
	v_fmac_f32_e32 v67, 0xba000000, v34
	v_fmac_f32_e32 v35, v67, v67
	v_fmac_f32_e32 v65, 0xba000000, v34
	v_fmac_f32_e32 v35, v65, v65
	v_fmac_f32_e32 v64, 0xba000000, v34
	v_fmac_f32_e32 v35, v64, v64
	v_fmac_f32_e32 v63, 0xba000000, v34
	v_fmac_f32_e32 v35, v63, v63
	v_fmac_f32_e32 v62, 0xba000000, v34
	v_fmac_f32_e32 v35, v62, v62
	v_fmac_f32_e32 v61, 0xba000000, v34
	v_fmac_f32_e32 v35, v61, v61
	v_fmac_f32_e32 v60, 0xba000000, v34
	v_fmac_f32_e32 v35, v60, v60
	v_fmac_f32_e32 v59, 0xba000000, v34
	v_fmac_f32_e32 v35, v59, v59
	v_fmac_f32_e32 v58, 0xba000000, v34
	v_fmac_f32_e32 v35, v58, v58
	v_fmac_f32_e32 v56, 0xba000000, v34
	v_fmac_f32_e32 v35, v56, v56
	v_fmac_f32_e32 v49, 0xba000000, v34
	v_fmac_f32_e32 v35, v49, v49
	v_fmac_f32_e32 v48, 0xba000000, v34
	v_fmac_f32_e32 v35, v48, v48
	v_fmac_f32_e32 v47, 0xba000000, v34
	v_fmac_f32_e32 v35, v47, v47
	v_fmac_f32_e32 v46, 0xba000000, v34
	v_fmac_f32_e32 v35, v46, v46
	v_fmac_f32_e32 v45, 0xba000000, v34
	v_fmac_f32_e32 v35, v45, v45
	v_fmac_f32_e32 v44, 0xba000000, v34
	v_fmac_f32_e32 v35, v44, v44
	v_fmac_f32_e32 v0, 0xba000000, v34
	v_fmac_f32_e32 v35, v0, v0
	ds_swizzle_b32 v34, v35 offset:swizzle(SWAP,1)
	s_waitcnt lgkmcnt(0)
	v_add_f32_e32 v34, v35, v34
	ds_swizzle_b32 v35, v34 offset:swizzle(SWAP,2)
	s_waitcnt lgkmcnt(0)
	v_add_f32_e32 v34, v34, v35
	ds_swizzle_b32 v35, v34 offset:swizzle(SWAP,4)
	s_waitcnt lgkmcnt(0)
	v_add_f32_e32 v34, v34, v35
	ds_swizzle_b32 v35, v34 offset:swizzle(SWAP,8)
	s_waitcnt lgkmcnt(0)
	v_add_f32_e32 v34, v34, v35
	ds_swizzle_b32 v35, v34 offset:swizzle(SWAP,16)
	s_waitcnt lgkmcnt(0)
	v_add_f32_e32 v34, v34, v35
	v_mov_b32_e32 v35, v34
	s_nop 1
	v_permlane32_swap_b32_e32 v34, v35
	v_add_f32_e32 v34, v34, v35
	v_fmamk_f32 v34, v34, 0x3a000000, v210
	v_cmp_gt_f32_e32 vcc, s25, v34
	v_mul_f32_e32 v35, 0x4f800000, v34
	s_nop 0
	v_cndmask_b32_e32 v34, v34, v35, vcc
	v_sqrt_f32_e32 v35, v34
	s_nop 0
	v_add_u32_e32 v36, -1, v35
	v_fma_f32 v37, -v36, v35, v34
	v_cmp_ge_f32_e64 s[58:59], 0, v37
	v_add_u32_e32 v37, 1, v35
	s_nop 0
	v_cndmask_b32_e64 v36, v35, v36, s[58:59]
	v_fma_f32 v35, -v37, v35, v34
	v_cmp_lt_f32_e64 s[58:59], 0, v35
	s_nop 1
	v_cndmask_b32_e64 v35, v36, v37, s[58:59]
	v_mul_f32_e32 v36, 0x37800000, v35
	v_cndmask_b32_e32 v35, v35, v36, vcc
	v_cmp_class_f32_e32 vcc, v34, v211
	s_nop 1
	v_cndmask_b32_e32 v34, v35, v34, vcc
	v_div_scale_f32 v35, s[20:21], v34, v34, 1.0
	v_rcp_f32_e32 v36, v35
	s_lshl_b64 s[20:21], s[62:63], 11
	v_lshl_add_u64 v[42:43], v[86:87], 0, s[20:21]
	v_fma_f32 v37, -v35, v36, 1.0
	v_fmac_f32_e32 v36, v37, v36
	v_div_scale_f32 v37, vcc, 1.0, v34, 1.0
	v_mul_f32_e32 v38, v37, v36
	v_fma_f32 v39, -v35, v38, v37
	v_fmac_f32_e32 v38, v39, v36
	v_fma_f32 v35, -v35, v38, v37
	v_div_fmas_f32 v35, v35, v36, v38
	v_div_fixup_f32 v57, v35, v34, 1.0
	v_mul_f32_e32 v108, v108, v57
	v_mul_f32_e32 v96, v96, v57
	v_mul_f32_e32 v99, v99, v57
	v_mul_f32_e32 v98, v98, v57
	v_mul_f32_e32 v97, v97, v57
	v_mul_f32_e32 v62, v62, v57
	v_mul_f32_e32 v65, v65, v57
	v_mul_f32_e32 v64, v64, v57
	v_mul_f32_e32 v63, v63, v57
	v_mul_f32_e32 v47, v47, v57
	v_mul_f32_e32 v56, v56, v57
	v_mul_f32_e32 v49, v49, v57
	v_mul_f32_e32 v48, v48, v57
	v_mul_f32_e32 v0, v0, v57
	s_waitcnt vmcnt(63)
	v_fma_f32 v104, v182, v108, v190
	v_mul_f32_e32 v38, v109, v57
	v_fma_f32 v105, v183, v38, v191
	v_mul_f32_e32 v39, v111, v57
	v_fma_f32 v41, v185, v39, v193
	v_mul_f32_e32 v39, v159, v57
	v_fma_f32 v39, v186, v39, v194
	v_mul_f32_e32 v34, v160, v57
	v_fma_f32 v35, v187, v34, v195
	v_mul_f32_e32 v34, v161, v57
	v_mul_f32_e32 v38, v110, v57
	v_fma_f32 v34, v188, v34, v196
	v_mul_f32_e32 v36, v162, v57
	v_cvt_pk_bf16_f32 v100, v104, v105
	v_fma_f32 v38, v184, v38, v192
	v_fma_f32 v37, v189, v36, v197
	v_cvt_pk_bf16_f32 v101, v38, v41
	v_cvt_pk_bf16_f32 v102, v39, v35
	v_cvt_pk_bf16_f32 v103, v34, v37
	global_store_dwordx4 v[54:55], v[100:103], off
	v_med3_f32 v36, v104, s19, v229
	v_med3_f32 v40, v105, s19, v229
	v_mov_b32_e32 v100, v1
	v_cvt_pk_fp8_f32 v100, v36, v40
	v_med3_f32 v36, v38, s19, v229
	v_med3_f32 v38, v41, s19, v229
	v_med3_f32 v35, v35, s19, v229
	v_cvt_pk_fp8_f32 v100, v36, v38 op_sel:[0,0,1]
	v_med3_f32 v36, v39, s19, v229
	v_mov_b32_e32 v101, v1
	v_cvt_pk_fp8_f32 v101, v36, v35
	v_med3_f32 v34, v34, s19, v229
	v_med3_f32 v35, v37, s19, v229
	v_cvt_pk_fp8_f32 v101, v34, v35 op_sel:[0,0,1]
	global_store_dwordx2 v[42:43], v[100:101], off
	s_nop 0
	s_waitcnt vmcnt(17)
	v_fma_f32 v107, v96, v201, v209
	v_mul_f32_e32 v41, v95, v57
	v_fma_f32 v41, v41, v202, v212
	v_mul_f32_e32 v34, v94, v57
	v_fma_f32 v94, v34, v203, v213
	v_mul_f32_e32 v34, v91, v57
	v_fma_f32 v91, v34, v204, v214
	v_mul_f32_e32 v34, v67, v57
	v_fma_f32 v38, v99, v198, v206
	v_fma_f32 v39, v98, v199, v207
	v_fma_f32 v40, v97, v200, v208
	v_fma_f32 v103, v34, v205, v215
	v_cvt_pk_bf16_f32 v34, v38, v39
	v_cvt_pk_bf16_f32 v35, v40, v107
	v_cvt_pk_bf16_f32 v36, v41, v94
	v_cvt_pk_bf16_f32 v37, v91, v103
	global_store_dwordx4 v[54:55], v[34:37], off offset:1024
	v_lshlrev_b32_e32 v67, 16, v31
	s_nop 0
	v_med3_f32 v35, v38, s19, v229
	v_med3_f32 v36, v39, s19, v229
	v_mov_b32_e32 v34, v1
	v_cvt_pk_fp8_f32 v34, v35, v36
	v_med3_f32 v35, v40, s19, v229
	v_med3_f32 v36, v107, s19, v229
	v_med3_f32 v37, v94, s19, v229
	v_cvt_pk_fp8_f32 v34, v35, v36 op_sel:[0,0,1]
	v_med3_f32 v36, v41, s19, v229
	v_mov_b32_e32 v35, v1
	v_cvt_pk_fp8_f32 v35, v36, v37
	v_med3_f32 v36, v91, s19, v229
	v_med3_f32 v37, v103, s19, v229
	v_and_b32_e32 v91, 0xffff0000, v31
	v_cvt_pk_fp8_f32 v35, v36, v37 op_sel:[0,0,1]
	global_store_dwordx2 v[42:43], v[34:35], off offset:512
	s_nop 0
	s_waitcnt vmcnt(16)
	v_fma_f32 v101, v62, v219, v227
	v_mul_f32_e32 v41, v61, v57
	v_fma_f32 v41, v41, v220, v240
	v_mul_f32_e32 v34, v60, v57
	v_fma_f32 v60, v34, v221, v241
	v_mul_f32_e32 v34, v59, v57
	v_fma_f32 v59, v34, v222, v242
	v_mul_f32_e32 v34, v58, v57
	v_fma_f32 v38, v65, v216, v224
	v_fma_f32 v39, v64, v217, v225
	v_fma_f32 v40, v63, v218, v226
	v_fma_f32 v97, v34, v223, v243
	v_cvt_pk_bf16_f32 v34, v38, v39
	v_cvt_pk_bf16_f32 v35, v40, v101
	v_cvt_pk_bf16_f32 v36, v41, v60
	v_cvt_pk_bf16_f32 v37, v59, v97
	global_store_dwordx4 v[54:55], v[34:37], off offset:2048
	v_lshlrev_b32_e32 v94, 16, v32
	v_and_b32_e32 v95, 0xffff0000, v32
	v_med3_f32 v35, v38, s19, v229
	v_med3_f32 v36, v39, s19, v229
	v_mov_b32_e32 v34, v1
	v_cvt_pk_fp8_f32 v34, v35, v36
	v_med3_f32 v35, v40, s19, v229
	v_med3_f32 v36, v101, s19, v229
	v_med3_f32 v37, v60, s19, v229
	v_cvt_pk_fp8_f32 v34, v35, v36 op_sel:[0,0,1]
	v_med3_f32 v36, v41, s19, v229
	v_mov_b32_e32 v35, v1
	v_cvt_pk_fp8_f32 v35, v36, v37
	v_med3_f32 v36, v59, s19, v229
	v_med3_f32 v37, v97, s19, v229
	v_lshlrev_b32_e32 v96, 16, v33
	v_cvt_pk_fp8_f32 v35, v36, v37 op_sel:[0,0,1]
	v_and_b32_e32 v97, 0xffff0000, v33
	v_add_f32_e32 v31, v96, v97
	v_and_b32_e32 v33, 0xffff0000, v18
	global_store_dwordx2 v[42:43], v[34:35], off offset:1024
	s_nop 0
	v_lshlrev_b32_e32 v32, 16, v19
	s_waitcnt vmcnt(63)
	v_fma_f32 v61, v0, v235, v251
	s_waitcnt vmcnt(19)
	v_fma_f32 v65, v47, v247, v239
	v_mul_f32_e32 v41, v46, v57
	v_fma_f32 v41, v41, v232, v248
	v_mul_f32_e32 v34, v45, v57
	v_fma_f32 v45, v34, v233, v249
	v_mul_f32_e32 v34, v44, v57
	v_fma_f32 v38, v56, v244, v236
	v_fma_f32 v39, v49, v245, v237
	v_fma_f32 v40, v48, v246, v238
	v_fma_f32 v44, v34, v234, v250
	v_cvt_pk_bf16_f32 v34, v38, v39
	v_cvt_pk_bf16_f32 v35, v40, v65
	v_cvt_pk_bf16_f32 v36, v41, v45
	v_cvt_pk_bf16_f32 v37, v44, v61
	global_store_dwordx4 v[54:55], v[34:37], off offset:3072
	v_med3_f32 v0, v38, s19, v229
	v_lshlrev_b32_e32 v64, 16, v30
	v_med3_f32 v35, v39, s19, v229
	v_mov_b32_e32 v34, v1
	v_cvt_pk_fp8_f32 v34, v0, v35
	v_med3_f32 v0, v40, s19, v229
	v_med3_f32 v35, v65, s19, v229
	v_med3_f32 v36, v45, s19, v229
	v_cvt_pk_fp8_f32 v34, v0, v35 op_sel:[0,0,1]
	v_med3_f32 v0, v41, s19, v229
	v_mov_b32_e32 v35, v1
	v_cvt_pk_fp8_f32 v35, v0, v36
	v_med3_f32 v0, v44, s19, v229
	v_med3_f32 v36, v61, s19, v229
	v_and_b32_e32 v65, 0xffff0000, v30
	v_cvt_pk_fp8_f32 v35, v0, v36 op_sel:[0,0,1]
	v_add_f32_e32 v0, v64, v65
	v_add_f32_e32 v30, v67, v91
	v_lshlrev_b32_e32 v55, 16, v26
	v_and_b32_e32 v54, 0xffff0000, v26
	v_lshlrev_b32_e32 v49, 16, v27
	v_and_b32_e32 v48, 0xffff0000, v27
	global_store_dwordx2 v[42:43], v[34:35], off offset:1536
	v_add_f32_e32 v0, v0, v30
	v_add_f32_e32 v30, v94, v95
	v_lshlrev_b32_e32 v47, 16, v28
	v_and_b32_e32 v46, 0xffff0000, v28
	v_lshlrev_b32_e32 v45, 16, v29
	v_and_b32_e32 v44, 0xffff0000, v29
	v_add_f32_e32 v26, v55, v54
	v_add_f32_e32 v27, v49, v48
	v_lshlrev_b32_e32 v43, 16, v22
	v_and_b32_e32 v42, 0xffff0000, v22
	v_lshlrev_b32_e32 v41, 16, v23
	v_and_b32_e32 v40, 0xffff0000, v23
	v_add_f32_e32 v30, v30, v31
	v_add_f32_e32 v26, v26, v27
	v_add_f32_e32 v27, v47, v46
	v_add_f32_e32 v28, v45, v44
	v_lshlrev_b32_e32 v39, 16, v24
	v_and_b32_e32 v38, 0xffff0000, v24
	v_lshlrev_b32_e32 v37, 16, v25
	v_and_b32_e32 v36, 0xffff0000, v25
	v_add_f32_e32 v22, v43, v42
	v_add_f32_e32 v23, v41, v40
	v_add_f32_e32 v0, v0, v30
	v_add_f32_e32 v27, v27, v28
	v_add_f32_e32 v22, v22, v23
	v_add_f32_e32 v23, v39, v38
	v_add_f32_e32 v24, v37, v36
	v_add_f32_e32 v0, 0, v0
	v_add_f32_e32 v26, v26, v27
	v_add_f32_e32 v23, v23, v24
	v_add_f32_e32 v0, v0, v26
	v_add_f32_e32 v22, v22, v23
	v_lshlrev_b32_e32 v34, 16, v18
	v_and_b32_e32 v31, 0xffff0000, v19
	v_add_f32_e32 v22, v0, v22
	v_lshlrev_b32_e32 v30, 16, v20
	v_and_b32_e32 v29, 0xffff0000, v20
	v_lshlrev_b32_e32 v28, 16, v21
	v_and_b32_e32 v0, 0xffff0000, v21
	v_add_f32_e32 v18, v34, v33
	v_add_f32_e32 v19, v32, v31
	v_add_f32_e32 v18, v18, v19
	v_add_f32_e32 v19, v30, v29
	v_add_f32_e32 v20, v28, v0
	v_add_f32_e32 v19, v19, v20
	v_add_f32_e32 v18, v18, v19
	v_add_f32_e32 v18, v22, v18
	ds_swizzle_b32 v19, v18 offset:swizzle(SWAP,1)
	s_waitcnt lgkmcnt(0)
	v_add_f32_e32 v18, v18, v19
	ds_swizzle_b32 v19, v18 offset:swizzle(SWAP,2)
	s_waitcnt lgkmcnt(0)
	v_add_f32_e32 v18, v18, v19
	ds_swizzle_b32 v19, v18 offset:swizzle(SWAP,4)
	s_waitcnt lgkmcnt(0)
	v_add_f32_e32 v18, v18, v19
	ds_swizzle_b32 v19, v18 offset:swizzle(SWAP,8)
	s_waitcnt lgkmcnt(0)
	v_add_f32_e32 v18, v18, v19
	ds_swizzle_b32 v19, v18 offset:swizzle(SWAP,16)
	s_waitcnt lgkmcnt(0)
	v_add_f32_e32 v18, v18, v19
	v_mov_b32_e32 v19, v18
	s_nop 1
	v_permlane32_swap_b32_e32 v18, v19
	v_add_f32_e32 v18, v18, v19
	v_fmac_f32_e32 v65, 0xba000000, v18
	v_fmac_f32_e32 v64, 0xba000000, v18
	v_mul_f32_e32 v19, v65, v65
	v_fmac_f32_e32 v19, v64, v64
	v_fmac_f32_e32 v67, 0xba000000, v18
	v_fmac_f32_e32 v19, v67, v67
	v_fmac_f32_e32 v91, 0xba000000, v18
	v_fmac_f32_e32 v19, v91, v91
	v_fmac_f32_e32 v94, 0xba000000, v18
	v_fmac_f32_e32 v19, v94, v94
	v_fmac_f32_e32 v95, 0xba000000, v18
	v_fmac_f32_e32 v19, v95, v95
	v_fmac_f32_e32 v96, 0xba000000, v18
	v_fmac_f32_e32 v19, v96, v96
	v_fmac_f32_e32 v97, 0xba000000, v18
	v_fmac_f32_e32 v19, v97, v97
	v_fmac_f32_e32 v55, 0xba000000, v18
	v_fmac_f32_e32 v19, v55, v55
	v_fmac_f32_e32 v54, 0xba000000, v18
	v_fmac_f32_e32 v19, v54, v54
	v_fmac_f32_e32 v49, 0xba000000, v18
	v_fmac_f32_e32 v19, v49, v49
	v_fmac_f32_e32 v48, 0xba000000, v18
	v_fmac_f32_e32 v19, v48, v48
	v_fmac_f32_e32 v47, 0xba000000, v18
	v_fmac_f32_e32 v19, v47, v47
	v_fmac_f32_e32 v46, 0xba000000, v18
	v_fmac_f32_e32 v19, v46, v46
	v_fmac_f32_e32 v45, 0xba000000, v18
	v_fmac_f32_e32 v19, v45, v45
	v_fmac_f32_e32 v44, 0xba000000, v18
	v_fmac_f32_e32 v19, v44, v44
	v_fmac_f32_e32 v43, 0xba000000, v18
	v_fmac_f32_e32 v19, v43, v43
	v_fmac_f32_e32 v42, 0xba000000, v18
	v_fmac_f32_e32 v19, v42, v42
	v_fmac_f32_e32 v41, 0xba000000, v18
	v_fmac_f32_e32 v19, v41, v41
	v_fmac_f32_e32 v40, 0xba000000, v18
	v_fmac_f32_e32 v19, v40, v40
	v_fmac_f32_e32 v39, 0xba000000, v18
	v_fmac_f32_e32 v19, v39, v39
	v_fmac_f32_e32 v38, 0xba000000, v18
	v_fmac_f32_e32 v19, v38, v38
	v_fmac_f32_e32 v37, 0xba000000, v18
	v_fmac_f32_e32 v19, v37, v37
	v_fmac_f32_e32 v36, 0xba000000, v18
	v_fmac_f32_e32 v19, v36, v36
	v_fmac_f32_e32 v34, 0xba000000, v18
	v_fmac_f32_e32 v19, v34, v34
	v_fmac_f32_e32 v33, 0xba000000, v18
	v_fmac_f32_e32 v19, v33, v33
	v_fmac_f32_e32 v32, 0xba000000, v18
	v_fmac_f32_e32 v19, v32, v32
	v_fmac_f32_e32 v31, 0xba000000, v18
	v_fmac_f32_e32 v19, v31, v31
	v_fmac_f32_e32 v30, 0xba000000, v18
	v_fmac_f32_e32 v19, v30, v30
	v_fmac_f32_e32 v29, 0xba000000, v18
	v_fmac_f32_e32 v19, v29, v29
	v_fmac_f32_e32 v28, 0xba000000, v18
	v_fmac_f32_e32 v19, v28, v28
	v_fmac_f32_e32 v0, 0xba000000, v18
	v_fmac_f32_e32 v19, v0, v0
	ds_swizzle_b32 v18, v19 offset:swizzle(SWAP,1)
	s_waitcnt lgkmcnt(0)
	v_add_f32_e32 v18, v19, v18
	ds_swizzle_b32 v19, v18 offset:swizzle(SWAP,2)
	s_waitcnt lgkmcnt(0)
	v_add_f32_e32 v18, v18, v19
	ds_swizzle_b32 v19, v18 offset:swizzle(SWAP,4)
	s_waitcnt lgkmcnt(0)
	v_add_f32_e32 v18, v18, v19
	ds_swizzle_b32 v19, v18 offset:swizzle(SWAP,8)
	s_waitcnt lgkmcnt(0)
	v_add_f32_e32 v18, v18, v19
	ds_swizzle_b32 v19, v18 offset:swizzle(SWAP,16)
	s_waitcnt lgkmcnt(0)
	v_add_f32_e32 v18, v18, v19
	v_mov_b32_e32 v19, v18
	s_nop 1
	v_permlane32_swap_b32_e32 v18, v19
	v_add_f32_e32 v18, v18, v19
	v_fmamk_f32 v18, v18, 0x3a000000, v210
	v_cmp_gt_f32_e32 vcc, s25, v18
	v_mul_f32_e32 v19, 0x4f800000, v18
	s_nop 0
	v_cndmask_b32_e32 v18, v18, v19, vcc
	v_sqrt_f32_e32 v19, v18
	s_nop 0
	v_add_u32_e32 v20, -1, v19
	v_fma_f32 v21, -v20, v19, v18
	v_cmp_ge_f32_e64 s[58:59], 0, v21
	v_add_u32_e32 v21, 1, v19
	s_nop 0
	v_cndmask_b32_e64 v20, v19, v20, s[58:59]
	v_fma_f32 v19, -v21, v19, v18
	v_cmp_lt_f32_e64 s[58:59], 0, v19
	s_nop 1
	v_cndmask_b32_e64 v19, v20, v21, s[58:59]
	v_mul_f32_e32 v20, 0x37800000, v19
	v_cndmask_b32_e32 v19, v19, v20, vcc
	v_cmp_class_f32_e32 vcc, v18, v211
	s_nop 1
	v_cndmask_b32_e32 v18, v19, v18, vcc
	v_div_scale_f32 v19, s[20:21], v18, v18, 1.0
	v_rcp_f32_e32 v20, v19
	s_lshl_b64 s[20:21], s[60:61], 11
	v_lshl_add_u64 v[26:27], v[86:87], 0, s[20:21]
	v_fma_f32 v21, -v19, v20, 1.0
	v_fmac_f32_e32 v20, v21, v20
	v_div_scale_f32 v21, vcc, 1.0, v18, 1.0
	v_mul_f32_e32 v22, v21, v20
	v_fma_f32 v23, -v19, v22, v21
	v_fmac_f32_e32 v22, v23, v20
	v_fma_f32 v19, -v19, v22, v21
	v_div_fmas_f32 v19, v19, v20, v22
	v_div_fixup_f32 v35, v19, v18, 1.0
	v_mul_f32_e32 v64, v64, v35
	v_mul_f32_e32 v48, v48, v35
	v_mul_f32_e32 v55, v55, v35
	v_mul_f32_e32 v54, v54, v35
	v_mul_f32_e32 v49, v49, v35
	v_mul_f32_e32 v40, v40, v35
	v_mul_f32_e32 v43, v43, v35
	v_mul_f32_e32 v42, v42, v35
	v_mul_f32_e32 v41, v41, v35
	v_mul_f32_e32 v31, v31, v35
	v_mul_f32_e32 v34, v34, v35
	v_mul_f32_e32 v33, v33, v35
	v_mul_f32_e32 v32, v32, v35
	v_mul_f32_e32 v0, v0, v35
	s_waitcnt vmcnt(63)
	v_fma_f32 v60, v182, v64, v190
	v_mul_f32_e32 v22, v65, v35
	v_fma_f32 v61, v183, v22, v191
	v_mul_f32_e32 v23, v91, v35
	v_fma_f32 v25, v185, v23, v193
	v_mul_f32_e32 v23, v94, v35
	v_fma_f32 v23, v186, v23, v194
	v_mul_f32_e32 v18, v95, v35
	v_fma_f32 v19, v187, v18, v195
	v_mul_f32_e32 v18, v96, v35
	v_mul_f32_e32 v22, v67, v35
	v_fma_f32 v18, v188, v18, v196
	v_mul_f32_e32 v20, v97, v35
	v_cvt_pk_bf16_f32 v56, v60, v61
	v_fma_f32 v22, v184, v22, v192
	v_fma_f32 v21, v189, v20, v197
	v_cvt_pk_bf16_f32 v57, v22, v25
	v_cvt_pk_bf16_f32 v58, v23, v19
	v_cvt_pk_bf16_f32 v59, v18, v21
	global_store_dwordx4 v[52:53], v[56:59], off
	v_med3_f32 v20, v60, s19, v229
	v_med3_f32 v24, v61, s19, v229
	v_mov_b32_e32 v56, v1
	v_cvt_pk_fp8_f32 v56, v20, v24
	v_med3_f32 v20, v22, s19, v229
	v_med3_f32 v22, v25, s19, v229
	v_med3_f32 v19, v19, s19, v229
	v_cvt_pk_fp8_f32 v56, v20, v22 op_sel:[0,0,1]
	v_med3_f32 v20, v23, s19, v229
	v_mov_b32_e32 v57, v1
	v_cvt_pk_fp8_f32 v57, v20, v19
	v_med3_f32 v18, v18, s19, v229
	v_med3_f32 v19, v21, s19, v229
	v_cvt_pk_fp8_f32 v57, v18, v19 op_sel:[0,0,1]
	global_store_dwordx2 v[26:27], v[56:57], off
	s_nop 0
	s_waitcnt vmcnt(18)
	v_fma_f32 v63, v48, v201, v209
	v_mul_f32_e32 v25, v47, v35
	v_fma_f32 v25, v25, v202, v212
	v_mul_f32_e32 v18, v46, v35
	v_fma_f32 v46, v18, v203, v213
	v_mul_f32_e32 v18, v45, v35
	v_fma_f32 v45, v18, v204, v214
	v_mul_f32_e32 v18, v44, v35
	v_fma_f32 v22, v55, v198, v206
	v_fma_f32 v23, v54, v199, v207
	v_fma_f32 v24, v49, v200, v208
	v_fma_f32 v59, v18, v205, v215
	v_cvt_pk_bf16_f32 v18, v22, v23
	v_cvt_pk_bf16_f32 v19, v24, v63
	v_cvt_pk_bf16_f32 v20, v25, v46
	v_cvt_pk_bf16_f32 v21, v45, v59
	global_store_dwordx4 v[52:53], v[18:21], off offset:1024
	v_lshlrev_b32_e32 v48, 16, v16
	v_and_b32_e32 v49, 0xffff0000, v16
	v_med3_f32 v19, v22, s19, v229
	v_med3_f32 v20, v23, s19, v229
	v_mov_b32_e32 v18, v1
	v_cvt_pk_fp8_f32 v18, v19, v20
	v_med3_f32 v19, v24, s19, v229
	v_med3_f32 v20, v63, s19, v229
	v_med3_f32 v21, v46, s19, v229
	v_cvt_pk_fp8_f32 v18, v19, v20 op_sel:[0,0,1]
	v_med3_f32 v20, v25, s19, v229
	v_mov_b32_e32 v19, v1
	v_cvt_pk_fp8_f32 v19, v20, v21
	v_med3_f32 v20, v45, s19, v229
	v_med3_f32 v21, v59, s19, v229
	v_lshlrev_b32_e32 v16, 16, v3
	v_cvt_pk_fp8_f32 v19, v20, v21 op_sel:[0,0,1]
	global_store_dwordx2 v[26:27], v[18:19], off offset:512
	s_nop 0
	s_waitcnt vmcnt(63)
	v_fma_f32 v57, v40, v219, v227
	v_mul_f32_e32 v25, v39, v35
	v_fma_f32 v25, v25, v220, v240
	v_mul_f32_e32 v18, v38, v35
	v_fma_f32 v38, v18, v221, v241
	v_mul_f32_e32 v18, v37, v35
	v_fma_f32 v37, v18, v222, v242
	v_mul_f32_e32 v18, v36, v35
	v_fma_f32 v22, v43, v216, v224
	v_fma_f32 v23, v42, v217, v225
	v_fma_f32 v24, v41, v218, v226
	v_fma_f32 v47, v18, v223, v243
	v_cvt_pk_bf16_f32 v18, v22, v23
	v_cvt_pk_bf16_f32 v19, v24, v57
	v_cvt_pk_bf16_f32 v20, v25, v38
	v_cvt_pk_bf16_f32 v21, v37, v47
	global_store_dwordx4 v[52:53], v[18:21], off offset:2048
	v_lshlrev_b32_e32 v44, 16, v14
	v_and_b32_e32 v45, 0xffff0000, v14
	v_med3_f32 v19, v22, s19, v229
	v_med3_f32 v20, v23, s19, v229
	v_mov_b32_e32 v18, v1
	v_cvt_pk_fp8_f32 v18, v19, v20
	v_med3_f32 v19, v24, s19, v229
	v_med3_f32 v20, v57, s19, v229
	v_med3_f32 v21, v38, s19, v229
	v_cvt_pk_fp8_f32 v18, v19, v20 op_sel:[0,0,1]
	v_med3_f32 v20, v25, s19, v229
	v_mov_b32_e32 v19, v1
	v_cvt_pk_fp8_f32 v19, v20, v21
	v_med3_f32 v20, v37, s19, v229
	v_med3_f32 v21, v47, s19, v229
	v_lshlrev_b32_e32 v46, 16, v15
	v_cvt_pk_fp8_f32 v19, v20, v21 op_sel:[0,0,1]
	v_and_b32_e32 v47, 0xffff0000, v15
	v_add_f32_e32 v14, v46, v47
	global_store_dwordx2 v[26:27], v[18:19], off offset:1024
	s_nop 0
	s_waitcnt vmcnt(63)
	v_fma_f32 v39, v0, v235, v251
	s_waitcnt vmcnt(23)
	v_fma_f32 v43, v31, v247, v239
	v_mul_f32_e32 v25, v30, v35
	v_fma_f32 v25, v25, v232, v248
	v_mul_f32_e32 v18, v29, v35
	v_fma_f32 v29, v18, v233, v249
	v_mul_f32_e32 v18, v28, v35
	v_fma_f32 v22, v34, v244, v236
	v_fma_f32 v23, v33, v245, v237
	v_fma_f32 v24, v32, v246, v238
	v_fma_f32 v28, v18, v234, v250
	v_cvt_pk_bf16_f32 v18, v22, v23
	v_cvt_pk_bf16_f32 v19, v24, v43
	v_cvt_pk_bf16_f32 v20, v25, v29
	v_cvt_pk_bf16_f32 v21, v28, v39
	global_store_dwordx4 v[52:53], v[18:21], off offset:3072
	v_med3_f32 v0, v22, s19, v229
	v_lshlrev_b32_e32 v52, 16, v17
	v_med3_f32 v19, v23, s19, v229
	v_mov_b32_e32 v18, v1
	v_cvt_pk_fp8_f32 v18, v0, v19
	v_med3_f32 v0, v24, s19, v229
	v_med3_f32 v19, v43, s19, v229
	v_med3_f32 v20, v29, s19, v229
	v_cvt_pk_fp8_f32 v18, v0, v19 op_sel:[0,0,1]
	v_med3_f32 v0, v25, s19, v229
	v_mov_b32_e32 v19, v1
	v_cvt_pk_fp8_f32 v19, v0, v20
	v_med3_f32 v0, v28, s19, v229
	v_med3_f32 v20, v39, s19, v229
	v_and_b32_e32 v53, 0xffff0000, v17
	v_cvt_pk_fp8_f32 v19, v0, v20 op_sel:[0,0,1]
	v_add_f32_e32 v0, v44, v45
	v_lshlrev_b32_e32 v35, 16, v10
	v_and_b32_e32 v34, 0xffff0000, v10
	v_lshlrev_b32_e32 v33, 16, v11
	v_and_b32_e32 v32, 0xffff0000, v11
	global_store_dwordx2 v[26:27], v[18:19], off offset:1536
	v_add_f32_e32 v0, v0, v14
	v_add_f32_e32 v14, v48, v49
	v_add_f32_e32 v15, v52, v53
	v_lshlrev_b32_e32 v31, 16, v12
	v_and_b32_e32 v30, 0xffff0000, v12
	v_lshlrev_b32_e32 v29, 16, v13
	v_and_b32_e32 v28, 0xffff0000, v13
	v_add_f32_e32 v10, v35, v34
	v_add_f32_e32 v11, v33, v32
	v_lshlrev_b32_e32 v27, 16, v6
	v_and_b32_e32 v26, 0xffff0000, v6
	v_lshlrev_b32_e32 v25, 16, v7
	v_and_b32_e32 v24, 0xffff0000, v7
	v_add_f32_e32 v14, v14, v15
	v_add_f32_e32 v10, v10, v11
	v_add_f32_e32 v11, v31, v30
	v_add_f32_e32 v12, v29, v28
	v_lshlrev_b32_e32 v23, 16, v8
	v_and_b32_e32 v22, 0xffff0000, v8
	v_lshlrev_b32_e32 v21, 16, v9
	v_and_b32_e32 v20, 0xffff0000, v9
	v_add_f32_e32 v6, v27, v26
	v_add_f32_e32 v7, v25, v24
	v_add_f32_e32 v0, v0, v14
	v_add_f32_e32 v11, v11, v12
	v_add_f32_e32 v6, v6, v7
	v_add_f32_e32 v7, v23, v22
	v_add_f32_e32 v8, v21, v20
	v_add_f32_e32 v0, 0, v0
	v_add_f32_e32 v10, v10, v11
	v_add_f32_e32 v7, v7, v8
	v_add_f32_e32 v0, v0, v10
	v_add_f32_e32 v6, v6, v7
	v_lshlrev_b32_e32 v18, 16, v2
	v_and_b32_e32 v17, 0xffff0000, v2
	v_and_b32_e32 v15, 0xffff0000, v3
	v_add_f32_e32 v6, v0, v6
	v_lshlrev_b32_e32 v14, 16, v4
	v_and_b32_e32 v13, 0xffff0000, v4
	v_lshlrev_b32_e32 v12, 16, v5
	v_and_b32_e32 v0, 0xffff0000, v5
	v_add_f32_e32 v2, v18, v17
	v_add_f32_e32 v3, v16, v15
	v_add_f32_e32 v2, v2, v3
	v_add_f32_e32 v3, v14, v13
	v_add_f32_e32 v4, v12, v0
	v_add_f32_e32 v3, v3, v4
	v_add_f32_e32 v2, v2, v3
	v_add_f32_e32 v2, v6, v2
	ds_swizzle_b32 v3, v2 offset:swizzle(SWAP,1)
	v_lshl_add_u64 v[10:11], v[86:87], 0, s[6:7]
	s_mov_b32 s6, 4
	s_waitcnt lgkmcnt(0)
	v_add_f32_e32 v2, v2, v3
	ds_swizzle_b32 v3, v2 offset:swizzle(SWAP,2)
	s_waitcnt lgkmcnt(0)
	v_add_f32_e32 v2, v2, v3
	ds_swizzle_b32 v3, v2 offset:swizzle(SWAP,4)
	s_waitcnt lgkmcnt(0)
	v_add_f32_e32 v2, v2, v3
	ds_swizzle_b32 v3, v2 offset:swizzle(SWAP,8)
	s_waitcnt lgkmcnt(0)
	v_add_f32_e32 v2, v2, v3
	ds_swizzle_b32 v3, v2 offset:swizzle(SWAP,16)
	s_waitcnt lgkmcnt(0)
	v_add_f32_e32 v2, v2, v3
	v_mov_b32_e32 v3, v2
	s_nop 1
	v_permlane32_swap_b32_e32 v2, v3
	v_add_f32_e32 v2, v2, v3
	v_fmac_f32_e32 v45, 0xba000000, v2
	v_fmac_f32_e32 v44, 0xba000000, v2
	v_mul_f32_e32 v3, v45, v45
	v_fmac_f32_e32 v3, v44, v44
	v_fmac_f32_e32 v46, 0xba000000, v2
	v_fmac_f32_e32 v3, v46, v46
	v_fmac_f32_e32 v47, 0xba000000, v2
	v_fmac_f32_e32 v3, v47, v47
	v_fmac_f32_e32 v48, 0xba000000, v2
	v_fmac_f32_e32 v3, v48, v48
	v_fmac_f32_e32 v49, 0xba000000, v2
	v_fmac_f32_e32 v3, v49, v49
	v_fmac_f32_e32 v52, 0xba000000, v2
	v_fmac_f32_e32 v3, v52, v52
	v_fmac_f32_e32 v53, 0xba000000, v2
	v_fmac_f32_e32 v3, v53, v53
	v_fmac_f32_e32 v35, 0xba000000, v2
	v_fmac_f32_e32 v3, v35, v35
	v_fmac_f32_e32 v34, 0xba000000, v2
	v_fmac_f32_e32 v3, v34, v34
	v_fmac_f32_e32 v33, 0xba000000, v2
	v_fmac_f32_e32 v3, v33, v33
	v_fmac_f32_e32 v32, 0xba000000, v2
	v_fmac_f32_e32 v3, v32, v32
	v_fmac_f32_e32 v31, 0xba000000, v2
	v_fmac_f32_e32 v3, v31, v31
	v_fmac_f32_e32 v30, 0xba000000, v2
	v_fmac_f32_e32 v3, v30, v30
	v_fmac_f32_e32 v29, 0xba000000, v2
	v_fmac_f32_e32 v3, v29, v29
	v_fmac_f32_e32 v28, 0xba000000, v2
	v_fmac_f32_e32 v3, v28, v28
	v_fmac_f32_e32 v27, 0xba000000, v2
	v_fmac_f32_e32 v3, v27, v27
	v_fmac_f32_e32 v26, 0xba000000, v2
	v_fmac_f32_e32 v3, v26, v26
	v_fmac_f32_e32 v25, 0xba000000, v2
	v_fmac_f32_e32 v3, v25, v25
	v_fmac_f32_e32 v24, 0xba000000, v2
	v_fmac_f32_e32 v3, v24, v24
	v_fmac_f32_e32 v23, 0xba000000, v2
	v_fmac_f32_e32 v3, v23, v23
	v_fmac_f32_e32 v22, 0xba000000, v2
	v_fmac_f32_e32 v3, v22, v22
	v_fmac_f32_e32 v21, 0xba000000, v2
	v_fmac_f32_e32 v3, v21, v21
	v_fmac_f32_e32 v20, 0xba000000, v2
	v_fmac_f32_e32 v3, v20, v20
	v_fmac_f32_e32 v18, 0xba000000, v2
	v_fmac_f32_e32 v3, v18, v18
	v_fmac_f32_e32 v17, 0xba000000, v2
	v_fmac_f32_e32 v3, v17, v17
	v_fmac_f32_e32 v16, 0xba000000, v2
	v_fmac_f32_e32 v3, v16, v16
	v_fmac_f32_e32 v15, 0xba000000, v2
	v_fmac_f32_e32 v3, v15, v15
	v_fmac_f32_e32 v14, 0xba000000, v2
	v_fmac_f32_e32 v3, v14, v14
	v_fmac_f32_e32 v13, 0xba000000, v2
	v_fmac_f32_e32 v3, v13, v13
	v_fmac_f32_e32 v12, 0xba000000, v2
	v_fmac_f32_e32 v3, v12, v12
	v_fmac_f32_e32 v0, 0xba000000, v2
	v_fmac_f32_e32 v3, v0, v0
	ds_swizzle_b32 v2, v3 offset:swizzle(SWAP,1)
	s_waitcnt lgkmcnt(0)
	v_add_f32_e32 v2, v3, v2
	ds_swizzle_b32 v3, v2 offset:swizzle(SWAP,2)
	s_waitcnt lgkmcnt(0)
	v_add_f32_e32 v2, v2, v3
	ds_swizzle_b32 v3, v2 offset:swizzle(SWAP,4)
	s_waitcnt lgkmcnt(0)
	v_add_f32_e32 v2, v2, v3
	ds_swizzle_b32 v3, v2 offset:swizzle(SWAP,8)
	s_waitcnt lgkmcnt(0)
	v_add_f32_e32 v2, v2, v3
	ds_swizzle_b32 v3, v2 offset:swizzle(SWAP,16)
	s_waitcnt lgkmcnt(0)
	v_add_f32_e32 v2, v2, v3
	v_mov_b32_e32 v3, v2
	s_nop 1
	v_permlane32_swap_b32_e32 v2, v3
	v_add_f32_e32 v2, v2, v3
	v_fmamk_f32 v2, v2, 0x3a000000, v210
	v_cmp_gt_f32_e32 vcc, s25, v2
	v_mul_f32_e32 v3, 0x4f800000, v2
	s_nop 0
	v_cndmask_b32_e32 v2, v2, v3, vcc
	v_sqrt_f32_e32 v3, v2
	s_nop 0
	v_add_u32_e32 v4, -1, v3
	v_fma_f32 v5, -v4, v3, v2
	v_cmp_ge_f32_e64 s[58:59], 0, v5
	v_add_u32_e32 v5, 1, v3
	s_nop 0
	v_cndmask_b32_e64 v4, v3, v4, s[58:59]
	v_fma_f32 v3, -v5, v3, v2
	v_cmp_lt_f32_e64 s[58:59], 0, v3
	s_nop 1
	v_cndmask_b32_e64 v3, v4, v5, s[58:59]
	v_mul_f32_e32 v4, 0x37800000, v3
	v_cndmask_b32_e32 v3, v3, v4, vcc
	v_cmp_class_f32_e32 vcc, v2, v211
	s_nop 1
	v_cndmask_b32_e32 v2, v3, v2, vcc
	v_div_scale_f32 v3, s[20:21], v2, v2, 1.0
	v_rcp_f32_e32 v4, v3
	s_nop 0
	v_fma_f32 v5, -v3, v4, 1.0
	v_fmac_f32_e32 v4, v5, v4
	v_div_scale_f32 v5, vcc, 1.0, v2, 1.0
	v_mul_f32_e32 v6, v5, v4
	v_fma_f32 v7, -v3, v6, v5
	v_fmac_f32_e32 v6, v7, v4
	v_fma_f32 v3, -v3, v6, v5
	v_div_fmas_f32 v3, v3, v4, v6
	v_div_fixup_f32 v19, v3, v2, 1.0
	v_mul_f32_e32 v44, v44, v19
	v_mul_f32_e32 v31, v31, v19
	v_mul_f32_e32 v35, v35, v19
	v_mul_f32_e32 v34, v34, v19
	v_mul_f32_e32 v33, v33, v19
	v_mul_f32_e32 v32, v32, v19
	v_mul_f32_e32 v23, v23, v19
	v_mul_f32_e32 v27, v27, v19
	v_mul_f32_e32 v26, v26, v19
	v_mul_f32_e32 v25, v25, v19
	v_mul_f32_e32 v24, v24, v19
	v_mul_f32_e32 v15, v15, v19
	v_mul_f32_e32 v18, v18, v19
	v_mul_f32_e32 v17, v17, v19
	v_mul_f32_e32 v16, v16, v19
	v_mul_f32_e32 v0, v0, v19
	s_and_b64 vcc, exec, s[4:5]
	s_mov_b64 s[4:5], 0
	s_waitcnt vmcnt(63)
	v_fma_f32 v40, v182, v44, v190
	v_mul_f32_e32 v6, v45, v19
	v_fma_f32 v41, v183, v6, v191
	v_mul_f32_e32 v7, v47, v19
	v_fma_f32 v9, v185, v7, v193
	v_mul_f32_e32 v7, v48, v19
	v_fma_f32 v7, v186, v7, v194
	v_mul_f32_e32 v2, v49, v19
	v_fma_f32 v3, v187, v2, v195
	v_mul_f32_e32 v2, v52, v19
	v_mul_f32_e32 v6, v46, v19
	v_fma_f32 v4, v188, v2, v196
	v_mul_f32_e32 v2, v53, v19
	v_cvt_pk_bf16_f32 v36, v40, v41
	v_fma_f32 v6, v184, v6, v192
	v_fma_f32 v5, v189, v2, v197
	v_cvt_pk_bf16_f32 v37, v6, v9
	v_cvt_pk_bf16_f32 v38, v7, v3
	v_cvt_pk_bf16_f32 v39, v4, v5
	global_store_dwordx4 v[50:51], v[36:39], off
	v_med3_f32 v8, v40, s19, v229
	v_mov_b32_e32 v2, v1
	v_med3_f32 v36, v41, s19, v229
	v_cvt_pk_fp8_f32 v2, v8, v36
	v_med3_f32 v6, v6, s19, v229
	v_med3_f32 v8, v9, s19, v229
	v_med3_f32 v4, v4, s19, v229
	v_cvt_pk_fp8_f32 v2, v6, v8 op_sel:[0,0,1]
	v_med3_f32 v6, v7, s19, v229
	v_med3_f32 v7, v3, s19, v229
	v_mov_b32_e32 v3, v1
	v_cvt_pk_fp8_f32 v3, v6, v7
	v_med3_f32 v5, v5, s19, v229
	v_cvt_pk_fp8_f32 v3, v4, v5 op_sel:[0,0,1]
	global_store_dwordx2 v[10:11], v[2:3], off
	s_nop 0
	s_waitcnt vmcnt(63)
	v_fma_f32 v31, v31, v202, v212
	v_mul_f32_e32 v2, v30, v19
	v_fma_f32 v3, v2, v203, v213
	v_mul_f32_e32 v2, v29, v19
	s_waitcnt vmcnt(63)
	v_fma_f32 v35, v35, v198, v206
	v_fma_f32 v34, v34, v199, v207
	v_fma_f32 v33, v33, v200, v208
	v_fma_f32 v43, v32, v201, v209
	v_fma_f32 v4, v2, v204, v214
	v_mul_f32_e32 v2, v28, v19
	v_cvt_pk_bf16_f32 v6, v35, v34
	v_cvt_pk_bf16_f32 v7, v33, v43
	v_fma_f32 v5, v2, v205, v215
	v_cvt_pk_bf16_f32 v8, v31, v3
	v_cvt_pk_bf16_f32 v9, v4, v5
	global_store_dwordx4 v[50:51], v[6:9], off offset:1024
	v_mov_b32_e32 v2, v1
	v_med3_f32 v4, v4, s19, v229
	v_med3_f32 v6, v35, s19, v229
	v_med3_f32 v7, v34, s19, v229
	v_cvt_pk_fp8_f32 v2, v6, v7
	v_med3_f32 v6, v33, s19, v229
	v_med3_f32 v7, v43, s19, v229
	v_med3_f32 v5, v5, s19, v229
	v_cvt_pk_fp8_f32 v2, v6, v7 op_sel:[0,0,1]
	v_med3_f32 v6, v31, s19, v229
	v_med3_f32 v7, v3, s19, v229
	v_mov_b32_e32 v3, v1
	v_cvt_pk_fp8_f32 v3, v6, v7
	v_cvt_pk_fp8_f32 v3, v4, v5 op_sel:[0,0,1]
	global_store_dwordx2 v[10:11], v[2:3], off offset:512
	s_nop 0
	s_waitcnt vmcnt(63)
	v_fma_f32 v23, v23, v220, v240
	v_mul_f32_e32 v2, v22, v19
	v_fma_f32 v3, v2, v221, v241
	v_mul_f32_e32 v2, v21, v19
	s_waitcnt vmcnt(63)
	v_fma_f32 v27, v27, v216, v224
	v_fma_f32 v26, v26, v217, v225
	v_fma_f32 v25, v25, v218, v226
	v_fma_f32 v35, v24, v219, v227
	v_fma_f32 v4, v2, v222, v242
	v_mul_f32_e32 v2, v20, v19
	v_cvt_pk_bf16_f32 v6, v27, v26
	v_cvt_pk_bf16_f32 v7, v25, v35
	v_fma_f32 v5, v2, v223, v243
	v_cvt_pk_bf16_f32 v8, v23, v3
	v_cvt_pk_bf16_f32 v9, v4, v5
	global_store_dwordx4 v[50:51], v[6:9], off offset:2048
	v_mov_b32_e32 v2, v1
	v_med3_f32 v4, v4, s19, v229
	v_med3_f32 v6, v27, s19, v229
	v_med3_f32 v7, v26, s19, v229
	v_cvt_pk_fp8_f32 v2, v6, v7
	v_med3_f32 v6, v25, s19, v229
	v_med3_f32 v7, v35, s19, v229
	v_med3_f32 v5, v5, s19, v229
	v_cvt_pk_fp8_f32 v2, v6, v7 op_sel:[0,0,1]
	v_med3_f32 v6, v23, s19, v229
	v_med3_f32 v7, v3, s19, v229
	v_mov_b32_e32 v3, v1
	v_cvt_pk_fp8_f32 v3, v6, v7
	v_cvt_pk_fp8_f32 v3, v4, v5 op_sel:[0,0,1]
	global_store_dwordx2 v[10:11], v[2:3], off offset:1024
	s_nop 0
	s_waitcnt vmcnt(63)
	v_fma_f32 v23, v0, v235, v251
	s_waitcnt vmcnt(63)
	v_fma_f32 v27, v15, v247, v239
	v_mul_f32_e32 v9, v14, v19
	v_fma_f32 v9, v9, v232, v248
	v_mul_f32_e32 v2, v13, v19
	v_fma_f32 v13, v2, v233, v249
	v_mul_f32_e32 v2, v12, v19
	v_fma_f32 v6, v18, v244, v236
	v_fma_f32 v7, v17, v245, v237
	v_fma_f32 v8, v16, v246, v238
	v_fma_f32 v12, v2, v234, v250
	v_cvt_pk_bf16_f32 v2, v6, v7
	v_cvt_pk_bf16_f32 v3, v8, v27
	v_cvt_pk_bf16_f32 v4, v9, v13
	v_cvt_pk_bf16_f32 v5, v12, v23
	global_store_dwordx4 v[50:51], v[2:5], off offset:3072
	v_med3_f32 v0, v6, s19, v229
	s_nop 0
	v_med3_f32 v3, v7, s19, v229
	v_mov_b32_e32 v2, v1
	v_cvt_pk_fp8_f32 v2, v0, v3
	v_med3_f32 v0, v8, s19, v229
	v_med3_f32 v3, v27, s19, v229
	v_med3_f32 v4, v13, s19, v229
	v_cvt_pk_fp8_f32 v2, v0, v3 op_sel:[0,0,1]
	v_med3_f32 v0, v9, s19, v229
	v_mov_b32_e32 v3, v1
	v_cvt_pk_fp8_f32 v3, v0, v4
	v_med3_f32 v0, v12, s19, v229
	v_med3_f32 v4, v23, s19, v229
	v_cvt_pk_fp8_f32 v3, v0, v4 op_sel:[0,0,1]
	global_store_dwordx2 v[10:11], v[2:3], off offset:1536
	s_cbranch_vccnz .LBB0_881
	v_mov_b32_e32 v234, 0xff800000
	v_mov_b32_e32 v235, 64
	v_mov_b64_e32 v[236:237], 0x200
	v_mov_b32_e32 v239, 0x3d800000
	v_mov_b64_e32 v[248:249], 0x1ff
	s_barrier
	s_and_saveexec_b64 s[4:5], s[56:57]
	ds_write_b32 v117, v1
	s_or_b64 exec, exec, s[4:5]
	v_ashrrev_i32_e32 v91, 31, v90
	v_lshlrev_b64 v[2:3], 12, v[90:91]
	v_lshl_add_u64 v[94:95], v[88:89], 0, v[2:3]
	v_mov_b32_e32 v2, 0
	s_mov_b64 s[4:5], 0
	v_mov_b32_e32 v3, v2
	v_mov_b32_e32 v4, v2
	v_mov_b32_e32 v5, v2
	v_mov_b32_e32 v6, v2
	v_mov_b32_e32 v7, v2
	v_mov_b32_e32 v8, v2
	v_mov_b32_e32 v9, v2
	v_mov_b32_e32 v10, v2
	v_mov_b32_e32 v11, v2
	v_mov_b32_e32 v12, v2
	v_mov_b32_e32 v13, v2
	v_mov_b32_e32 v14, v2
	v_mov_b32_e32 v15, v2
	v_mov_b32_e32 v16, v2
	v_mov_b32_e32 v17, v2
	v_mov_b32_e32 v18, v2
	v_mov_b32_e32 v19, v2
	v_mov_b32_e32 v20, v2
	v_mov_b32_e32 v21, v2
	v_mov_b32_e32 v22, v2
	v_mov_b32_e32 v23, v2
	v_mov_b32_e32 v24, v2
	v_mov_b32_e32 v25, v2
	v_mov_b32_e32 v38, v2
	v_mov_b32_e32 v39, v2
	v_mov_b32_e32 v40, v2
	v_mov_b32_e32 v41, v2
	v_mov_b32_e32 v50, v2
	v_mov_b32_e32 v51, v2
	v_mov_b32_e32 v52, v2
	v_mov_b32_e32 v53, v2
	v_mov_b32_e32 v26, v2
	v_mov_b32_e32 v27, v2
	v_mov_b32_e32 v28, v2
	v_mov_b32_e32 v29, v2
	v_mov_b32_e32 v30, v2
	v_mov_b32_e32 v31, v2
	v_mov_b32_e32 v32, v2
	v_mov_b32_e32 v33, v2
	v_mov_b32_e32 v34, v2
	v_mov_b32_e32 v35, v2
	v_mov_b32_e32 v36, v2
	v_mov_b32_e32 v37, v2
	v_mov_b32_e32 v42, v2
	v_mov_b32_e32 v43, v2
	v_mov_b32_e32 v44, v2
	v_mov_b32_e32 v45, v2
	v_mov_b32_e32 v46, v2
	v_mov_b32_e32 v47, v2
	v_mov_b32_e32 v48, v2
	v_mov_b32_e32 v49, v2
	v_mov_b32_e32 v54, v2
	v_mov_b32_e32 v55, v2
	v_mov_b32_e32 v56, v2
	v_mov_b32_e32 v57, v2
	v_mov_b32_e32 v58, v2
	v_mov_b32_e32 v59, v2
	v_mov_b32_e32 v60, v2
	v_mov_b32_e32 v61, v2
	v_mov_b32_e32 v62, v2
	v_mov_b32_e32 v63, v2
	v_mov_b32_e32 v64, v2
	v_mov_b32_e32 v65, v2
